# tail converter loops: done-counter load issued with the claim (one wait) instead of after it
# speedup vs baseline: 1.0058x; 1.0058x over previous
.LBB0_351:
	s_cmp_gt_u32 s24, 0x3fffffff
	s_cselect_b64 s[48:49], -1, 0
	s_ashr_i32 s57, s56, 31
	s_lshl_b64 s[8:9], s[56:57], 2
	v_add_u32_e32 v8, s26, v1
	s_add_u32 s8, s50, s8
	s_addc_u32 s9, s51, s9
	v_ashrrev_i32_e32 v4, 31, v8
	v_lshl_add_u64 v[2:3], s[8:9], 0, v[194:195]
	v_mul_lo_u32 v9, s54, v4
	v_mul_lo_u32 v6, s55, v8
	v_mad_u64_u32 v[4:5], s[8:9], s54, v8, 0
	v_add3_u32 v5, v5, v9, v6
	v_or_b32_e32 v6, 1, v8
	v_mul_lo_u32 v10, s55, v6
	v_mad_u64_u32 v[6:7], s[8:9], s54, v6, 0
	v_lshl_add_u64 v[4:5], v[4:5], 2, v[2:3]
	v_add3_u32 v7, v7, v9, v10
	v_lshl_add_u64 v[6:7], v[6:7], 2, v[2:3]
	global_load_dwordx4 v[58:61], v[4:5], off nt
	global_load_dwordx4 v[42:45], v[4:5], off offset:256 nt
	global_load_dwordx4 v[62:65], v[6:7], off nt
	global_load_dwordx4 v[46:49], v[6:7], off offset:256 nt
	v_add_u32_e32 v4, 64, v8
	v_ashrrev_i32_e32 v5, 31, v4
	v_mul_lo_u32 v6, s54, v5
	v_mul_lo_u32 v7, s55, v4
	v_mad_u64_u32 v[4:5], s[8:9], s54, v4, 0
	v_add3_u32 v5, v5, v6, v7
	v_add_u32_e32 v6, 0x41, v8
	v_ashrrev_i32_e32 v7, 31, v6
	v_mul_lo_u32 v8, s54, v7
	v_mul_lo_u32 v9, s55, v6
	v_mad_u64_u32 v[6:7], s[8:9], s54, v6, 0
	s_ashr_i32 s65, s64, 31
	s_lshl_b64 s[8:9], s[64:65], 2
	v_lshl_add_u64 v[4:5], v[4:5], 2, v[2:3]
	v_add3_u32 v7, v7, v8, v9
	v_add_u32_e32 v8, s44, v1
	s_add_u32 s8, s58, s8
	v_lshl_add_u64 v[2:3], v[6:7], 2, v[2:3]
	global_load_dwordx4 v[50:53], v[4:5], off nt
	global_load_dwordx4 v[34:37], v[4:5], off offset:256 nt
	global_load_dwordx4 v[54:57], v[2:3], off nt
	global_load_dwordx4 v[38:41], v[2:3], off offset:256 nt
	s_addc_u32 s9, s59, s9
	v_ashrrev_i32_e32 v4, 31, v8
	v_lshl_add_u64 v[2:3], s[8:9], 0, v[194:195]
	v_mul_lo_u32 v9, s60, v4
	v_mul_lo_u32 v6, s61, v8
	v_mad_u64_u32 v[4:5], s[8:9], s60, v8, 0
	v_add3_u32 v5, v5, v9, v6
	v_or_b32_e32 v6, 1, v8
	v_mul_lo_u32 v10, s61, v6
	v_mad_u64_u32 v[6:7], s[8:9], s60, v6, 0
	v_lshl_add_u64 v[4:5], v[4:5], 2, v[2:3]
	v_add3_u32 v7, v7, v9, v10
	v_lshl_add_u64 v[6:7], v[6:7], 2, v[2:3]
	global_load_dwordx4 v[26:29], v[4:5], off nt
	global_load_dwordx4 v[10:13], v[4:5], off offset:256 nt
	global_load_dwordx4 v[30:33], v[6:7], off nt
	global_load_dwordx4 v[14:17], v[6:7], off offset:256 nt
	v_add_u32_e32 v4, 64, v8
	v_ashrrev_i32_e32 v5, 31, v4
	v_mul_lo_u32 v6, s60, v5
	v_mul_lo_u32 v7, s61, v4
	v_mad_u64_u32 v[4:5], s[8:9], s60, v4, 0
	v_add3_u32 v5, v5, v6, v7
	v_add_u32_e32 v6, 0x41, v8
	v_ashrrev_i32_e32 v7, 31, v6
	v_mul_lo_u32 v8, s60, v7
	v_mul_lo_u32 v9, s61, v6
	v_mad_u64_u32 v[6:7], s[8:9], s60, v6, 0
	v_add3_u32 v7, v7, v8, v9
	v_lshl_add_u64 v[4:5], v[4:5], 2, v[2:3]
	v_lshl_add_u64 v[6:7], v[6:7], 2, v[2:3]
	global_load_dwordx4 v[18:21], v[4:5], off nt
	s_nop 0
	global_load_dwordx4 v[2:5], v[4:5], off offset:256 nt
	s_nop 0
	global_load_dwordx4 v[22:25], v[6:7], off nt
	s_nop 0
	global_load_dwordx4 v[6:9], v[6:7], off offset:256 nt
	s_nor_b64 s[24:25], s[42:43], s[48:49]
	v_mov_b32_e32 v100, 0
	v_mov_b32_e32 v77, 0
	v_mov_b32_e32 v76, 0
	s_and_saveexec_b64 s[8:9], s[24:25]
	s_cbranch_execz .LBB0_355
	global_load_dword v100, v195, s[4:5] sc1
	s_mov_b64 s[54:55], exec
	v_mbcnt_lo_u32_b32 v76, s54, 0
	v_mbcnt_hi_u32_b32 v76, s55, v76
	v_cmp_eq_u32_e32 vcc, 0, v76
	s_and_saveexec_b64 s[50:51], vcc
	s_cbranch_execz .LBB0_354
	s_bcnt1_i32_b64 s24, s[54:55]
	s_lshl_b32 s24, s24, 1
	v_mov_b32_e32 v77, s24
	global_atomic_add v77, v195, v77, s[6:7] sc0
.LBB0_354:
	s_or_b64 exec, exec, s[50:51]
	s_waitcnt vmcnt(0)
	v_readfirstlane_b32 s24, v77
	s_nop 0
	v_lshl_add_u32 v76, v76, 1, s24

.LBB0_372:
	s_movk_i32 s2, 0x4c3f
	v_cmp_gt_u32_e64 s[44:45], s66, v100
	v_cmp_lt_u32_e32 vcc, s2, v76
	s_or_b64 s[8:9], s[48:49], vcc
	v_cndmask_b32_e64 v2, 2.0, 0, s[44:45]
	v_or_b32_e32 v2, v2, v76
	v_readlane_b32 s2, v254, 44
	v_cndmask_b32_e64 v2, v2, -1, s[8:9]
	s_nop 0
	v_mov_b32_e32 v3, s2
	ds_write_b32 v3, v2
	s_branch .LBB0_328

.LBB0_517:
	s_cmp_gt_u32 s18, 0x3fffffff
	s_cselect_b64 s[48:49], -1, 0
	s_ashr_i32 s57, s56, 31
	s_lshl_b64 s[8:9], s[56:57], 2
	v_add_u32_e32 v8, s28, v1
	s_add_u32 s8, s50, s8
	s_addc_u32 s9, s51, s9
	v_ashrrev_i32_e32 v4, 31, v8
	v_lshl_add_u64 v[2:3], s[8:9], 0, v[194:195]
	v_mul_lo_u32 v9, s54, v4
	v_mul_lo_u32 v6, s55, v8
	v_mad_u64_u32 v[4:5], s[8:9], s54, v8, 0
	v_add3_u32 v5, v5, v9, v6
	v_or_b32_e32 v6, 1, v8
	v_mul_lo_u32 v10, s55, v6
	v_mad_u64_u32 v[6:7], s[8:9], s54, v6, 0
	v_lshl_add_u64 v[4:5], v[4:5], 2, v[2:3]
	v_add3_u32 v7, v7, v9, v10
	v_lshl_add_u64 v[6:7], v[6:7], 2, v[2:3]
	global_load_dwordx4 v[58:61], v[4:5], off nt
	global_load_dwordx4 v[42:45], v[4:5], off offset:256 nt
	global_load_dwordx4 v[62:65], v[6:7], off nt
	global_load_dwordx4 v[46:49], v[6:7], off offset:256 nt
	v_add_u32_e32 v4, 64, v8
	v_ashrrev_i32_e32 v5, 31, v4
	v_mul_lo_u32 v6, s54, v5
	v_mul_lo_u32 v7, s55, v4
	v_mad_u64_u32 v[4:5], s[8:9], s54, v4, 0
	v_add3_u32 v5, v5, v6, v7
	v_add_u32_e32 v6, 0x41, v8
	v_ashrrev_i32_e32 v7, 31, v6
	v_mul_lo_u32 v8, s54, v7
	v_mul_lo_u32 v9, s55, v6
	v_mad_u64_u32 v[6:7], s[8:9], s54, v6, 0
	s_ashr_i32 s65, s64, 31
	s_lshl_b64 s[8:9], s[64:65], 2
	v_lshl_add_u64 v[4:5], v[4:5], 2, v[2:3]
	v_add3_u32 v7, v7, v8, v9
	v_add_u32_e32 v8, s44, v1
	s_add_u32 s8, s58, s8
	v_lshl_add_u64 v[2:3], v[6:7], 2, v[2:3]
	global_load_dwordx4 v[50:53], v[4:5], off nt
	global_load_dwordx4 v[34:37], v[4:5], off offset:256 nt
	global_load_dwordx4 v[54:57], v[2:3], off nt
	global_load_dwordx4 v[38:41], v[2:3], off offset:256 nt
	s_addc_u32 s9, s59, s9
	v_ashrrev_i32_e32 v4, 31, v8
	v_lshl_add_u64 v[2:3], s[8:9], 0, v[194:195]
	v_mul_lo_u32 v9, s60, v4
	v_mul_lo_u32 v6, s61, v8
	v_mad_u64_u32 v[4:5], s[8:9], s60, v8, 0
	v_add3_u32 v5, v5, v9, v6
	v_or_b32_e32 v6, 1, v8
	v_mul_lo_u32 v10, s61, v6
	v_mad_u64_u32 v[6:7], s[8:9], s60, v6, 0
	v_lshl_add_u64 v[4:5], v[4:5], 2, v[2:3]
	v_add3_u32 v7, v7, v9, v10
	v_lshl_add_u64 v[6:7], v[6:7], 2, v[2:3]
	global_load_dwordx4 v[26:29], v[4:5], off nt
	global_load_dwordx4 v[10:13], v[4:5], off offset:256 nt
	global_load_dwordx4 v[30:33], v[6:7], off nt
	global_load_dwordx4 v[14:17], v[6:7], off offset:256 nt
	v_add_u32_e32 v4, 64, v8
	v_ashrrev_i32_e32 v5, 31, v4
	v_mul_lo_u32 v6, s60, v5
	v_mul_lo_u32 v7, s61, v4
	v_mad_u64_u32 v[4:5], s[8:9], s60, v4, 0
	v_add3_u32 v5, v5, v6, v7
	v_add_u32_e32 v6, 0x41, v8
	v_ashrrev_i32_e32 v7, 31, v6
	v_mul_lo_u32 v8, s60, v7
	v_mul_lo_u32 v9, s61, v6
	v_mad_u64_u32 v[6:7], s[8:9], s60, v6, 0
	v_add3_u32 v7, v7, v8, v9
	v_lshl_add_u64 v[4:5], v[4:5], 2, v[2:3]
	v_lshl_add_u64 v[6:7], v[6:7], 2, v[2:3]
	global_load_dwordx4 v[18:21], v[4:5], off nt
	s_nop 0
	global_load_dwordx4 v[2:5], v[4:5], off offset:256 nt
	s_nop 0
	global_load_dwordx4 v[22:25], v[6:7], off nt
	s_nop 0
	global_load_dwordx4 v[6:9], v[6:7], off offset:256 nt
	s_nor_b64 s[18:19], s[42:43], s[48:49]
	v_mov_b32_e32 v100, 0
	v_mov_b32_e32 v77, 0
	v_mov_b32_e32 v76, 0
	s_and_saveexec_b64 s[8:9], s[18:19]
	s_cbranch_execz .LBB0_521
	global_load_dword v100, v195, s[26:27] offset:512 sc1
	s_mov_b64 s[54:55], exec
	v_mbcnt_lo_u32_b32 v76, s54, 0
	v_mbcnt_hi_u32_b32 v76, s55, v76
	v_cmp_eq_u32_e32 vcc, 0, v76
	s_and_saveexec_b64 s[50:51], vcc
	s_cbranch_execz .LBB0_520
	s_bcnt1_i32_b64 s18, s[54:55]
	s_lshl_b32 s18, s18, 1
	v_mov_b32_e32 v77, s18
	global_atomic_add v77, v195, v77, s[6:7] sc0
.LBB0_520:
	s_or_b64 exec, exec, s[50:51]
	s_waitcnt vmcnt(0)
	v_readfirstlane_b32 s18, v77
	s_nop 0
	v_lshl_add_u32 v76, v76, 1, s18

.LBB0_538:
	s_movk_i32 s2, 0x4c3f
	v_cmp_gt_u32_e64 s[44:45], s81, v100
	v_cmp_lt_u32_e32 vcc, s2, v76
	s_or_b64 s[18:19], s[48:49], vcc
	v_cndmask_b32_e64 v2, 2.0, 0, s[44:45]
	v_or_b32_e32 v2, v2, v76
	v_readlane_b32 s2, v254, 44
	v_cndmask_b32_e64 v2, v2, -1, s[18:19]
	s_nop 0
	v_mov_b32_e32 v3, s2
	ds_write_b32 v3, v2
	s_branch .LBB0_494

.LBB0_1047:
	s_cmp_gt_u32 s24, 0x3fffffff
	s_cselect_b64 s[56:57], -1, 0
	s_ashr_i32 s65, s64, 31
	s_lshl_b64 s[8:9], s[64:65], 2
	v_add_u32_e32 v8, s26, v1
	s_add_u32 s8, s58, s8
	s_addc_u32 s9, s59, s9
	v_ashrrev_i32_e32 v4, 31, v8
	v_lshl_add_u64 v[2:3], s[8:9], 0, v[194:195]
	v_mul_lo_u32 v9, s62, v4
	v_mul_lo_u32 v6, s63, v8
	v_mad_u64_u32 v[4:5], s[8:9], s62, v8, 0
	v_add3_u32 v5, v5, v9, v6
	v_or_b32_e32 v6, 1, v8
	v_mul_lo_u32 v10, s63, v6
	v_mad_u64_u32 v[6:7], s[8:9], s62, v6, 0
	v_lshl_add_u64 v[4:5], v[4:5], 2, v[2:3]
	v_add3_u32 v7, v7, v9, v10
	v_lshl_add_u64 v[6:7], v[6:7], 2, v[2:3]
	global_load_dwordx4 v[58:61], v[4:5], off nt
	global_load_dwordx4 v[42:45], v[4:5], off offset:256 nt
	global_load_dwordx4 v[62:65], v[6:7], off nt
	global_load_dwordx4 v[46:49], v[6:7], off offset:256 nt
	v_add_u32_e32 v4, 64, v8
	v_ashrrev_i32_e32 v5, 31, v4
	v_mul_lo_u32 v6, s62, v5
	v_mul_lo_u32 v7, s63, v4
	v_mad_u64_u32 v[4:5], s[8:9], s62, v4, 0
	v_add3_u32 v5, v5, v6, v7
	v_add_u32_e32 v6, 0x41, v8
	v_ashrrev_i32_e32 v7, 31, v6
	v_mul_lo_u32 v8, s62, v7
	v_mul_lo_u32 v9, s63, v6
	v_mad_u64_u32 v[6:7], s[8:9], s62, v6, 0
	s_ashr_i32 s73, s72, 31
	s_lshl_b64 s[8:9], s[72:73], 2
	v_lshl_add_u64 v[4:5], v[4:5], 2, v[2:3]
	v_add3_u32 v7, v7, v8, v9
	v_add_u32_e32 v8, s38, v1
	s_add_u32 s8, s66, s8
	v_lshl_add_u64 v[2:3], v[6:7], 2, v[2:3]
	global_load_dwordx4 v[50:53], v[4:5], off nt
	global_load_dwordx4 v[34:37], v[4:5], off offset:256 nt
	global_load_dwordx4 v[54:57], v[2:3], off nt
	global_load_dwordx4 v[38:41], v[2:3], off offset:256 nt
	s_addc_u32 s9, s67, s9
	v_ashrrev_i32_e32 v4, 31, v8
	v_lshl_add_u64 v[2:3], s[8:9], 0, v[194:195]
	v_mul_lo_u32 v9, s68, v4
	v_mul_lo_u32 v6, s69, v8
	v_mad_u64_u32 v[4:5], s[8:9], s68, v8, 0
	v_add3_u32 v5, v5, v9, v6
	v_or_b32_e32 v6, 1, v8
	v_mul_lo_u32 v10, s69, v6
	v_mad_u64_u32 v[6:7], s[8:9], s68, v6, 0
	v_lshl_add_u64 v[4:5], v[4:5], 2, v[2:3]
	v_add3_u32 v7, v7, v9, v10
	v_lshl_add_u64 v[6:7], v[6:7], 2, v[2:3]
	global_load_dwordx4 v[26:29], v[4:5], off nt
	global_load_dwordx4 v[10:13], v[4:5], off offset:256 nt
	global_load_dwordx4 v[30:33], v[6:7], off nt
	global_load_dwordx4 v[14:17], v[6:7], off offset:256 nt
	v_add_u32_e32 v4, 64, v8
	v_ashrrev_i32_e32 v5, 31, v4
	v_mul_lo_u32 v6, s68, v5
	v_mul_lo_u32 v7, s69, v4
	v_mad_u64_u32 v[4:5], s[8:9], s68, v4, 0
	v_add3_u32 v5, v5, v6, v7
	v_add_u32_e32 v6, 0x41, v8
	v_ashrrev_i32_e32 v7, 31, v6
	v_mul_lo_u32 v8, s68, v7
	v_mul_lo_u32 v9, s69, v6
	v_mad_u64_u32 v[6:7], s[8:9], s68, v6, 0
	v_add3_u32 v7, v7, v8, v9
	v_lshl_add_u64 v[4:5], v[4:5], 2, v[2:3]
	v_lshl_add_u64 v[6:7], v[6:7], 2, v[2:3]
	global_load_dwordx4 v[18:21], v[4:5], off nt
	s_nop 0
	global_load_dwordx4 v[2:5], v[4:5], off offset:256 nt
	s_nop 0
	global_load_dwordx4 v[22:25], v[6:7], off nt
	s_nop 0
	global_load_dwordx4 v[6:9], v[6:7], off offset:256 nt
	s_nor_b64 s[24:25], s[42:43], s[56:57]
	v_mov_b32_e32 v100, 0
	v_mov_b32_e32 v77, 0
	v_mov_b32_e32 v76, 0
	s_and_saveexec_b64 s[8:9], s[24:25]
	s_cbranch_execz .LBB0_1051
	global_load_dword v100, v195, s[6:7] offset:768 sc1
	s_mov_b64 s[62:63], exec
	v_mbcnt_lo_u32_b32 v76, s62, 0
	v_mbcnt_hi_u32_b32 v76, s63, v76
	v_cmp_eq_u32_e32 vcc, 0, v76
	s_and_saveexec_b64 s[58:59], vcc
	s_cbranch_execz .LBB0_1050
	s_bcnt1_i32_b64 s24, s[62:63]
	s_lshl_b32 s24, s24, 1
	v_mov_b32_e32 v77, s24
	global_atomic_add v77, v195, v77, s[4:5] sc0
.LBB0_1050:
	s_or_b64 exec, exec, s[58:59]
	s_waitcnt vmcnt(0)
	v_readfirstlane_b32 s24, v77
	s_nop 0
	v_lshl_add_u32 v76, v76, 1, s24

.LBB0_1068:
	s_movk_i32 s2, 0x4c3f
	v_cmp_gt_u32_e64 s[44:45], s81, v100
	v_cmp_lt_u32_e32 vcc, s2, v76
	s_or_b64 s[22:23], s[56:57], vcc
	v_cndmask_b32_e64 v2, 2.0, 0, s[44:45]
	v_or_b32_e32 v2, v2, v76
	v_readlane_b32 s2, v254, 44
	v_cndmask_b32_e64 v2, v2, -1, s[22:23]
	s_nop 0
	v_mov_b32_e32 v3, s2
	ds_write_b32 v3, v2
	s_branch .LBB0_1024

.LBB0_1233:
	s_cmp_gt_u32 s24, 0x3fffffff
	s_cselect_b64 s[56:57], -1, 0
	s_ashr_i32 s65, s64, 31
	s_lshl_b64 s[8:9], s[64:65], 2
	v_add_u32_e32 v8, s36, v1
	s_add_u32 s8, s58, s8
	s_addc_u32 s9, s59, s9
	v_ashrrev_i32_e32 v4, 31, v8
	v_lshl_add_u64 v[2:3], s[8:9], 0, v[194:195]
	v_mul_lo_u32 v9, s62, v4
	v_mul_lo_u32 v6, s63, v8
	v_mad_u64_u32 v[4:5], s[8:9], s62, v8, 0
	v_add3_u32 v5, v5, v9, v6
	v_or_b32_e32 v6, 1, v8
	v_mul_lo_u32 v10, s63, v6
	v_mad_u64_u32 v[6:7], s[8:9], s62, v6, 0
	v_lshl_add_u64 v[4:5], v[4:5], 2, v[2:3]
	v_add3_u32 v7, v7, v9, v10
	v_lshl_add_u64 v[6:7], v[6:7], 2, v[2:3]
	global_load_dwordx4 v[58:61], v[4:5], off nt
	global_load_dwordx4 v[42:45], v[4:5], off offset:256 nt
	global_load_dwordx4 v[62:65], v[6:7], off nt
	global_load_dwordx4 v[46:49], v[6:7], off offset:256 nt
	v_add_u32_e32 v4, 64, v8
	v_ashrrev_i32_e32 v5, 31, v4
	v_mul_lo_u32 v6, s62, v5
	v_mul_lo_u32 v7, s63, v4
	v_mad_u64_u32 v[4:5], s[8:9], s62, v4, 0
	v_add3_u32 v5, v5, v6, v7
	v_add_u32_e32 v6, 0x41, v8
	v_ashrrev_i32_e32 v7, 31, v6
	v_mul_lo_u32 v8, s62, v7
	v_mul_lo_u32 v9, s63, v6
	v_mad_u64_u32 v[6:7], s[8:9], s62, v6, 0
	s_ashr_i32 s73, s72, 31
	s_lshl_b64 s[8:9], s[72:73], 2
	v_lshl_add_u64 v[4:5], v[4:5], 2, v[2:3]
	v_add3_u32 v7, v7, v8, v9
	v_add_u32_e32 v8, s52, v1
	s_add_u32 s8, s66, s8
	v_lshl_add_u64 v[2:3], v[6:7], 2, v[2:3]
	global_load_dwordx4 v[50:53], v[4:5], off nt
	global_load_dwordx4 v[34:37], v[4:5], off offset:256 nt
	global_load_dwordx4 v[54:57], v[2:3], off nt
	global_load_dwordx4 v[38:41], v[2:3], off offset:256 nt
	s_addc_u32 s9, s67, s9
	v_ashrrev_i32_e32 v4, 31, v8
	v_lshl_add_u64 v[2:3], s[8:9], 0, v[194:195]
	v_mul_lo_u32 v9, s68, v4
	v_mul_lo_u32 v6, s69, v8
	v_mad_u64_u32 v[4:5], s[8:9], s68, v8, 0
	v_add3_u32 v5, v5, v9, v6
	v_or_b32_e32 v6, 1, v8
	v_mul_lo_u32 v10, s69, v6
	v_mad_u64_u32 v[6:7], s[8:9], s68, v6, 0
	v_lshl_add_u64 v[4:5], v[4:5], 2, v[2:3]
	v_add3_u32 v7, v7, v9, v10
	v_lshl_add_u64 v[6:7], v[6:7], 2, v[2:3]
	global_load_dwordx4 v[26:29], v[4:5], off nt
	global_load_dwordx4 v[10:13], v[4:5], off offset:256 nt
	global_load_dwordx4 v[30:33], v[6:7], off nt
	global_load_dwordx4 v[14:17], v[6:7], off offset:256 nt
	v_add_u32_e32 v4, 64, v8
	v_ashrrev_i32_e32 v5, 31, v4
	v_mul_lo_u32 v6, s68, v5
	v_mul_lo_u32 v7, s69, v4
	v_mad_u64_u32 v[4:5], s[8:9], s68, v4, 0
	v_add3_u32 v5, v5, v6, v7
	v_add_u32_e32 v6, 0x41, v8
	v_ashrrev_i32_e32 v7, 31, v6
	v_mul_lo_u32 v8, s68, v7
	v_mul_lo_u32 v9, s69, v6
	v_mad_u64_u32 v[6:7], s[8:9], s68, v6, 0
	v_add3_u32 v7, v7, v8, v9
	v_lshl_add_u64 v[4:5], v[4:5], 2, v[2:3]
	v_lshl_add_u64 v[6:7], v[6:7], 2, v[2:3]
	global_load_dwordx4 v[18:21], v[4:5], off nt
	s_nop 0
	global_load_dwordx4 v[2:5], v[4:5], off offset:256 nt
	s_nop 0
	global_load_dwordx4 v[22:25], v[6:7], off nt
	s_nop 0
	global_load_dwordx4 v[6:9], v[6:7], off offset:256 nt
	s_nor_b64 s[24:25], s[42:43], s[56:57]
	v_mov_b32_e32 v100, 0
	v_mov_b32_e32 v77, 0
	v_mov_b32_e32 v76, 0
	s_and_saveexec_b64 s[8:9], s[24:25]
	s_cbranch_execz .LBB0_1237
	global_load_dword v100, v195, s[6:7] sc1
	s_mov_b64 s[62:63], exec
	v_mbcnt_lo_u32_b32 v76, s62, 0
	v_mbcnt_hi_u32_b32 v76, s63, v76
	v_cmp_eq_u32_e32 vcc, 0, v76
	s_and_saveexec_b64 s[58:59], vcc
	s_cbranch_execz .LBB0_1236
	s_bcnt1_i32_b64 s24, s[62:63]
	s_lshl_b32 s24, s24, 1
	v_mov_b32_e32 v77, s24
	global_atomic_add v77, v195, v77, s[46:47] sc0

.LBB0_1254:
	s_movk_i32 s2, 0x4c3f
	v_cmp_gt_u32_e64 s[44:45], s81, v100
	v_cmp_lt_u32_e32 vcc, s2, v76
	s_or_b64 s[24:25], s[56:57], vcc
	v_cndmask_b32_e64 v2, 2.0, 0, s[44:45]
	v_or_b32_e32 v2, v2, v76
	v_readlane_b32 s2, v254, 44
	v_cndmask_b32_e64 v2, v2, -1, s[24:25]
	s_nop 0
	v_mov_b32_e32 v3, s2
	ds_write_b32 v3, v2
	s_branch .LBB0_1210
